# baseline (speedup 1.0000x reference)
.LBB1_236:
	v_cmp_gt_i32_e32 vcc, s93, v0
	s_and_b64 s[4:5], s[78:79], vcc
	s_waitcnt lgkmcnt(0)
	s_barrier
	s_and_saveexec_b64 s[0:1], s[4:5]
	s_cbranch_execz .LBB1_239
	v_add_u32_e32 v30, v37, v36
	v_add_u32_e32 v30, v30, v34
	v_add_u32_e32 v30, v30, v35
	v_add_u32_e32 v30, v30, v0
	v_ashrrev_i32_e32 v31, 31, v30
	v_lshl_add_u64 v[32:33], v[30:31], 2, s[74:75]
	s_mov_b64 s[4:5], 0
	s_mov_b64 s[14:15], 0x1000
.LBB1_238:
	v_add_u32_e32 v35, 0x100, v0
	v_add_u32_e32 v36, 0x200, v0
	v_add_u32_e32 v37, 0x300, v0
	v_cmp_gt_i32_e64 s[6:7], s93, v35
	v_cmp_gt_i32_e64 s[8:9], s93, v36
	v_cmp_gt_i32_e64 s[10:11], s93, v37
	ds_read_b32 v34, v1
	s_mov_b64 s[12:13], exec
	s_mov_b64 exec, s[6:7]
	ds_read_b32 v35, v1 offset:1024
	s_mov_b64 exec, s[8:9]
	ds_read_b32 v36, v1 offset:2048
	s_mov_b64 exec, s[10:11]
	ds_read_b32 v37, v1 offset:3072
	s_mov_b64 exec, s[12:13]
	v_add_u32_e32 v0, 0x400, v0
	v_add_u32_e32 v1, 0x1000, v1
	v_cmp_le_i32_e32 vcc, s93, v0
	s_or_b64 s[4:5], vcc, s[4:5]
	s_waitcnt lgkmcnt(0)
	global_store_dword v[32:33], v34, off nt
	s_mov_b64 exec, s[6:7]
	global_store_dword v[32:33], v35, off offset:1024 nt
	s_mov_b64 exec, s[8:9]
	global_store_dword v[32:33], v36, off offset:2048 nt
	s_mov_b64 exec, s[10:11]
	global_store_dword v[32:33], v37, off offset:3072 nt
	s_mov_b64 exec, s[12:13]
	v_lshl_add_u64 v[32:33], v[32:33], 0, s[14:15]
	s_andn2_b64 exec, exec, s[4:5]
	s_cbranch_execnz .LBB1_238

.LBB1_241:
	s_or_b64 exec, exec, s[0:1]
	v_or_b32_e32 v17, v87, v85
	s_mov_b32 s0, 0x186a0
	v_lshlrev_b32_e32 v0, 1, v82
	v_cmp_gt_i32_e32 vcc, s0, v86
	v_lshl_add_u64 v[0:1], s[82:83], 0, v[0:1]
	v_add_u32_e32 v14, s33, v17
	v_lshlrev_b32_e32 v16, 2, v17
	ds_read_b128 v[18:21], v16 offset:36624
	ds_read_b128 v[22:25], v16 offset:36880
	ds_read_b128 v[26:29], v78 offset:37136
	s_mov_b32 s0, 0x18660
	v_cmp_gt_i32_e64 s[0:1], s0, v86
	v_add_u32_e32 v30, s33, v85
	v_ashrrev_i32_e32 v15, 31, v14
	v_lshlrev_b64 v[32:33], 5, v[14:15]
	v_add_u32_e32 v30, 0x80, v30
	v_lshl_add_u64 v[32:33], v[0:1], 0, v[32:33]
	v_ashrrev_i32_e32 v31, 31, v30
	v_lshlrev_b64 v[34:35], 5, v[30:31]
	v_lshl_add_u64 v[34:35], v[0:1], 0, v[34:35]
	s_waitcnt lgkmcnt(0)
	v_fma_mixlo_f16 v2, v2, v18, 0
	v_fma_mixlo_f16 v3, v3, v19, 0
	v_fma_mixlo_f16 v4, v4, v20, 0
	v_fma_mixlo_f16 v5, v5, v21, 0
	v_fma_mixlo_f16 v6, v6, v22, 0
	v_fma_mixlo_f16 v7, v7, v23, 0
	v_fma_mixlo_f16 v8, v8, v24, 0
	v_fma_mixlo_f16 v9, v9, v25, 0
	v_fma_mixlo_f16 v10, v10, v26, 0
	v_fma_mixlo_f16 v11, v11, v27, 0
	v_fma_mixlo_f16 v12, v12, v28, 0
	v_fma_mixlo_f16 v13, v13, v29, 0
	s_and_saveexec_b64 s[4:5], vcc
	global_store_short v[32:33], v2, off
	global_store_short v[32:33], v3, off offset:32
	global_store_short v[32:33], v4, off offset:64
	global_store_short v[32:33], v5, off offset:96
	s_or_b64 exec, exec, s[4:5]
	s_and_saveexec_b64 s[4:5], s[0:1]
	global_store_short v[32:33], v6, off offset:2048
	global_store_short v[32:33], v7, off offset:2080
	global_store_short v[32:33], v8, off offset:2112
	global_store_short v[32:33], v9, off offset:2144
	s_or_b64 exec, exec, s[4:5]
	s_and_saveexec_b64 s[4:5], s[2:3]
	global_store_short v[34:35], v10, off
	global_store_short v[34:35], v11, off offset:32
	global_store_short v[34:35], v12, off offset:64
	global_store_short v[34:35], v13, off offset:96
	s_endpgm
